# speedup vs baseline: 1.0631x; 1.0018x over previous
_Z10agg_kernelPKDF16_PKiS2_S2_PKfS2_PDF16_Pfi:
	s_load_dwordx8 s[12:19], s[0:1], 0x0
	s_lshl_b32 s4, s2, 1
	s_ashr_i32 s5, s4, 31
	s_lshl_b64 s[4:5], s[4:5], 2
	v_and_b32_e32 v1, 63, v0
	s_waitcnt lgkmcnt(0)
	s_add_u32 s20, s16, s4
	s_addc_u32 s21, s17, s5
	s_load_dwordx2 s[16:17], s[20:21], 0x0
	s_load_dwordx8 s[4:11], s[0:1], 0x20
	v_readfirstlane_b32 s3, v0
	v_lshlrev_b32_e32 v2, 2, v1
	s_lshr_b32 s3, s3, 6
	s_waitcnt lgkmcnt(0)
	s_ashr_i32 s21, s16, 31
	s_mov_b32 s20, s16
	global_load_dword v3, v2, s[6:7]
	global_load_dword v4, v2, s[6:7] offset:256
	global_load_dword v6, v2, s[6:7] offset:512
	global_load_dword v5, v2, s[6:7] offset:768
	s_lshl_b64 s[6:7], s[20:21], 2
	s_add_u32 s6, s14, s6
	s_addc_u32 s7, s15, s7
	s_add_i32 s21, s17, 15
	s_ashr_i32 s21, s21, 4
	s_max_i32 s20, s21, 1
	s_add_i32 s20, s20, -1
	s_min_u32 s14, s3, s20
	s_bfe_u32 s44, s2, 0x10002
	s_mul_i32 s45, s44, s20
	s_lshl_b32 s44, s44, 1
	s_sub_i32 s44, 1, s44
	s_mul_i32 s14, s14, s44
	s_add_i32 s14, s14, s45
	s_lshl_b32 s30, s14, 4
	v_mov_b32_e32 v59, 0x30e0000
	v_bfe_u32 v2, v0, 4, 2
	v_lshlrev_b32_e32 v7, 2, v0
	s_lshl_b32 s14, s14, 6
	v_and_or_b32 v18, v7, 12, v2
	s_add_u32 s14, s6, s14
	s_addc_u32 s15, s7, 0
	v_lshlrev_b32_e32 v2, 2, v18
	global_load_dword v2, v2, s[14:15]
	v_lshlrev_b32_e32 v20, 2, v18
	v_mov_b32_e32 v8, 0
	v_mov_b32_e32 v9, 0
	v_mov_b32_e32 v10, 0
	v_mov_b32_e32 v11, 0
	v_lshlrev_b32_e32 v12, 4, v0
	v_add_u32_e32 v13, 0x10000, v12
	ds_write_b128 v12, v[8:11]
	ds_write_b128 v12, v[8:11] offset:16384
	ds_write_b128 v12, v[8:11] offset:32768
	ds_write_b128 v12, v[8:11] offset:49152
	ds_write_b128 v13, v[8:11]
	ds_write_b128 v13, v[8:11] offset:16384
	ds_write_b128 v13, v[8:11] offset:32768
	v_cmp_gt_u32_e32 vcc, 0x28c, v0
	s_and_saveexec_b64 s[14:15], vcc
	ds_write_b128 v13, v[8:11] offset:49152
	s_or_b64 exec, exec, s[14:15]
	s_waitcnt vmcnt(2)
	v_max3_i32 v3, v3, v4, v6
	v_mbcnt_lo_u32_b32 v4, -1, 0
	v_mbcnt_hi_u32_b32 v4, -1, v4
	v_and_b32_e32 v25, 64, v4
	s_waitcnt vmcnt(1)
	v_max3_i32 v3, v3, v5, 0
	v_add_u32_e32 v5, 64, v25
	v_xor_b32_e32 v6, 1, v4
	v_cmp_lt_i32_e32 vcc, v6, v5
	s_load_dword s16, s[0:1], 0x40
	s_mul_i32 s14, s2, 0x187
	v_cndmask_b32_e32 v6, v4, v6, vcc
	v_lshlrev_b32_e32 v6, 2, v6
	ds_bpermute_b32 v6, v6, v3
	s_waitcnt lgkmcnt(0)
	s_sub_i32 s15, s16, s14
	s_movk_i32 s0, 0x73
	s_cmp_gt_i32 s21, s3
	s_cselect_b64 s[22:23], -1, 0
	v_max_i32_e32 v3, v3, v6
	v_xor_b32_e32 v6, 2, v4
	v_cmp_lt_i32_e32 vcc, v6, v5
	v_mov_b32_e32 v29, 0
	v_mov_b32_e32 v27, 0
	v_cndmask_b32_e32 v6, v4, v6, vcc
	v_lshlrev_b32_e32 v6, 2, v6
	ds_bpermute_b32 v6, v6, v3
	v_mov_b32_e32 v28, 0
	v_mov_b32_e32 v26, 0
	v_mov_b32_e32 v21, 0
	s_waitcnt vmcnt(0)
	v_add_u32_e32 v33, s30, v18
	v_cmp_gt_i32_e64 s[28:29], s17, v33
	s_nop 1
	v_cndmask_b32_e64 v2, v59, v2, s[28:29]
	s_nop 1
	v_mov_b32_dpp v29, v2 row_newbcast:0 row_mask:0xf bank_mask:0xf
	s_waitcnt lgkmcnt(0)
	v_max_i32_e32 v3, v3, v6
	v_xor_b32_e32 v6, 4, v4
	v_cmp_lt_i32_e32 vcc, v6, v5
	v_mov_b32_dpp v27, v2 row_newbcast:1 row_mask:0xf bank_mask:0xf
	v_mov_b32_dpp v28, v2 row_newbcast:2 row_mask:0xf bank_mask:0xf
	v_cndmask_b32_e32 v6, v4, v6, vcc
	v_lshlrev_b32_e32 v6, 2, v6
	ds_bpermute_b32 v6, v6, v3
	v_mov_b32_dpp v26, v2 row_newbcast:3 row_mask:0xf bank_mask:0xf
	s_waitcnt lgkmcnt(0)
	s_barrier
	v_max_i32_e32 v3, v3, v6
	v_xor_b32_e32 v6, 8, v4
	v_cmp_lt_i32_e32 vcc, v6, v5
	s_nop 1
	v_cndmask_b32_e32 v6, v4, v6, vcc
	v_lshlrev_b32_e32 v60, 2, v6
	ds_bpermute_b32 v6, v60, v3
	s_waitcnt lgkmcnt(0)
	v_max_i32_e32 v3, v3, v6
	v_xor_b32_e32 v6, 16, v4
	v_cmp_lt_i32_e32 vcc, v6, v5
	s_nop 1
	v_cndmask_b32_e32 v6, v4, v6, vcc
	v_lshlrev_b32_e32 v61, 2, v6
	ds_bpermute_b32 v6, v61, v3
	s_waitcnt lgkmcnt(0)
	v_max_i32_e32 v3, v3, v6
	v_xor_b32_e32 v6, 32, v4
	v_cmp_lt_i32_e32 vcc, v6, v5
	v_and_b32_e32 v5, 15, v0
	v_lshlrev_b32_e32 v24, 4, v5
	v_cndmask_b32_e32 v4, v4, v6, vcc
	v_lshlrev_b32_e32 v66, 2, v4
	ds_bpermute_b32 v4, v66, v3
	v_lshlrev_b32_e32 v23, 2, v5
	s_waitcnt lgkmcnt(0)
	v_max_i32_e32 v3, v3, v4
	v_lshrrev_b32_e32 v3, 23, v3
	v_mov_b32_e32 v4, 0x8b
	v_med3_u32 v3, v3, s0, v4
	s_sub_i32 s0, s21, s3
	s_add_i32 s0, s0, 15
	s_cmp_gt_u32 s0, 15
	s_cselect_b64 s[24:25], -1, 0
	v_lshlrev_b32_e32 v19, 23, v3
	s_and_b64 s[22:23], s[22:23], s[24:25]
	v_sub_u32_e32 v22, 0x84800000, v19
	s_and_b64 vcc, exec, s[22:23]
	s_cbranch_vccz .LBB2_5
	s_lshr_b32 s21, s0, 4
	s_mov_b32 s1, 0
	s_mov_b32 s22, 0x1ffff00
	s_mov_b32 s23, 0x4b400000
	v_lshl_add_u64 v[20:21], s[6:7], 0, v[20:21]
	s_add_i32 s0, s3, 16
	s_mov_b32 s24, s0
	s_min_i32 s24, s24, s20
	s_mul_i32 s24, s24, s44
	s_add_i32 s24, s24, s45
	s_lshl_b32 s24, s24, 4
	s_ashr_i32 s25, s24, 31
	v_lshl_add_u64 v[32:33], s[24:25], 2, v[20:21]
	global_load_dword v30, v[32:33], off
	v_lshlrev_b32_e32 v35, 8, v29
	v_and_or_b32 v35, v35, s22, v24
	global_load_dwordx4 v[2:5], v35, s[12:13]
	v_lshlrev_b32_e32 v35, 8, v27
	v_and_or_b32 v35, v35, s22, v24
	global_load_dwordx4 v[6:9], v35, s[12:13]
	v_lshlrev_b32_e32 v35, 8, v28
	v_and_or_b32 v35, v35, s22, v24
	global_load_dwordx4 v[10:13], v35, s[12:13]
	v_lshlrev_b32_e32 v35, 8, v26
	v_and_or_b32 v35, v35, s22, v24
	global_load_dwordx4 v[14:17], v35, s[12:13]
.Lagg_loop:
	s_waitcnt vmcnt(4)
	s_mov_b32 s24, s0
	s_min_i32 s24, s24, s20
	s_mul_i32 s24, s24, s44
	s_add_i32 s24, s24, s45
	s_lshl_b32 s24, s24, 4
	v_add_u32_e32 v33, s24, v18
	v_cmp_gt_i32_e64 s[28:29], s17, v33
	s_add_i32 s24, s0, 16
	s_min_i32 s24, s24, s20
	s_mul_i32 s24, s24, s44
	s_add_i32 s24, s24, s45
	s_lshl_b32 s24, s24, 4
	s_ashr_i32 s25, s24, 31
	v_cndmask_b32_e64 v31, v59, v30, s[28:29]
	v_lshl_add_u64 v[32:33], s[24:25], 2, v[20:21]
	global_load_dword v30, v[32:33], off
	s_waitcnt vmcnt(4)
	v_ashrrev_i32_e32 v32, 17, v29
	v_mul_i32_i24_e32 v32, 0x140, v32
	v_fma_mix_f32 v33, v2, v22, s23 op_sel_hi:[1,0,0]
	v_fma_mix_f32 v34, v2, v22, s23 op_sel:[1,0,0] op_sel_hi:[1,0,0]
	v_or_b32_e32 v32, v23, v32
	v_lshl_add_u32 v33, v34, 16, v33
	ds_add_u32 v32, v33
	v_fma_mix_f32 v33, v3, v22, s23 op_sel_hi:[1,0,0]
	v_fma_mix_f32 v34, v3, v22, s23 op_sel:[1,0,0] op_sel_hi:[1,0,0]
	s_nop 0
	v_lshl_add_u32 v33, v34, 16, v33
	ds_add_u32 v32, v33 offset:64
	v_fma_mix_f32 v33, v4, v22, s23 op_sel_hi:[1,0,0]
	v_fma_mix_f32 v34, v4, v22, s23 op_sel:[1,0,0] op_sel_hi:[1,0,0]
	s_nop 0
	v_lshl_add_u32 v33, v34, 16, v33
	ds_add_u32 v32, v33 offset:128
	v_fma_mix_f32 v33, v5, v22, s23 op_sel_hi:[1,0,0]
	v_fma_mix_f32 v34, v5, v22, s23 op_sel:[1,0,0] op_sel_hi:[1,0,0]
	s_nop 0
	v_lshl_add_u32 v33, v34, 16, v33
	ds_add_u32 v32, v33 offset:192
	v_mov_b32_e32 v29, 0
	s_nop 1
	v_mov_b32_dpp v29, v31 row_newbcast:0 row_mask:0xf bank_mask:0xf
	v_lshlrev_b32_e32 v35, 8, v29
	v_and_or_b32 v35, v35, s22, v24
	s_waitcnt vmcnt(1)
	global_load_dwordx4 v[2:5], v35, s[12:13]
	s_waitcnt vmcnt(4)
	v_ashrrev_i32_e32 v32, 17, v27
	v_mul_i32_i24_e32 v32, 0x140, v32
	v_fma_mix_f32 v33, v6, v22, s23 op_sel_hi:[1,0,0]
	v_fma_mix_f32 v34, v6, v22, s23 op_sel:[1,0,0] op_sel_hi:[1,0,0]
	v_or_b32_e32 v32, v23, v32
	v_lshl_add_u32 v33, v34, 16, v33
	ds_add_u32 v32, v33
	v_fma_mix_f32 v33, v7, v22, s23 op_sel_hi:[1,0,0]
	v_fma_mix_f32 v34, v7, v22, s23 op_sel:[1,0,0] op_sel_hi:[1,0,0]
	s_nop 0
	v_lshl_add_u32 v33, v34, 16, v33
	ds_add_u32 v32, v33 offset:64
	v_fma_mix_f32 v33, v8, v22, s23 op_sel_hi:[1,0,0]
	v_fma_mix_f32 v34, v8, v22, s23 op_sel:[1,0,0] op_sel_hi:[1,0,0]
	s_nop 0
	v_lshl_add_u32 v33, v34, 16, v33
	ds_add_u32 v32, v33 offset:128
	v_fma_mix_f32 v33, v9, v22, s23 op_sel_hi:[1,0,0]
	v_fma_mix_f32 v34, v9, v22, s23 op_sel:[1,0,0] op_sel_hi:[1,0,0]
	s_nop 0
	v_lshl_add_u32 v33, v34, 16, v33
	ds_add_u32 v32, v33 offset:192
	v_mov_b32_e32 v27, 0
	s_nop 1
	v_mov_b32_dpp v27, v31 row_newbcast:1 row_mask:0xf bank_mask:0xf
	v_lshlrev_b32_e32 v35, 8, v27
	v_and_or_b32 v35, v35, s22, v24
	s_waitcnt vmcnt(1)
	global_load_dwordx4 v[6:9], v35, s[12:13]
	s_waitcnt vmcnt(4)
	v_ashrrev_i32_e32 v32, 17, v28
	v_mul_i32_i24_e32 v32, 0x140, v32
	v_fma_mix_f32 v33, v10, v22, s23 op_sel_hi:[1,0,0]
	v_fma_mix_f32 v34, v10, v22, s23 op_sel:[1,0,0] op_sel_hi:[1,0,0]
	v_or_b32_e32 v32, v23, v32
	v_lshl_add_u32 v33, v34, 16, v33
	ds_add_u32 v32, v33
	v_fma_mix_f32 v33, v11, v22, s23 op_sel_hi:[1,0,0]
	v_fma_mix_f32 v34, v11, v22, s23 op_sel:[1,0,0] op_sel_hi:[1,0,0]
	s_nop 0
	v_lshl_add_u32 v33, v34, 16, v33
	ds_add_u32 v32, v33 offset:64
	v_fma_mix_f32 v33, v12, v22, s23 op_sel_hi:[1,0,0]
	v_fma_mix_f32 v34, v12, v22, s23 op_sel:[1,0,0] op_sel_hi:[1,0,0]
	s_nop 0
	v_lshl_add_u32 v33, v34, 16, v33
	ds_add_u32 v32, v33 offset:128
	v_fma_mix_f32 v33, v13, v22, s23 op_sel_hi:[1,0,0]
	v_fma_mix_f32 v34, v13, v22, s23 op_sel:[1,0,0] op_sel_hi:[1,0,0]
	s_nop 0
	v_lshl_add_u32 v33, v34, 16, v33
	ds_add_u32 v32, v33 offset:192
	v_mov_b32_e32 v28, 0
	s_nop 1
	v_mov_b32_dpp v28, v31 row_newbcast:2 row_mask:0xf bank_mask:0xf
	v_lshlrev_b32_e32 v35, 8, v28
	v_and_or_b32 v35, v35, s22, v24
	s_waitcnt vmcnt(1)
	global_load_dwordx4 v[10:13], v35, s[12:13]
	s_waitcnt vmcnt(4)
	v_ashrrev_i32_e32 v32, 17, v26
	v_mul_i32_i24_e32 v32, 0x140, v32
	v_fma_mix_f32 v33, v14, v22, s23 op_sel_hi:[1,0,0]
	v_fma_mix_f32 v34, v14, v22, s23 op_sel:[1,0,0] op_sel_hi:[1,0,0]
	v_or_b32_e32 v32, v23, v32
	v_lshl_add_u32 v33, v34, 16, v33
	ds_add_u32 v32, v33
	v_fma_mix_f32 v33, v15, v22, s23 op_sel_hi:[1,0,0]
	v_fma_mix_f32 v34, v15, v22, s23 op_sel:[1,0,0] op_sel_hi:[1,0,0]
	s_nop 0
	v_lshl_add_u32 v33, v34, 16, v33
	ds_add_u32 v32, v33 offset:64
	v_fma_mix_f32 v33, v16, v22, s23 op_sel_hi:[1,0,0]
	v_fma_mix_f32 v34, v16, v22, s23 op_sel:[1,0,0] op_sel_hi:[1,0,0]
	s_nop 0
	v_lshl_add_u32 v33, v34, 16, v33
	ds_add_u32 v32, v33 offset:128
	v_fma_mix_f32 v33, v17, v22, s23 op_sel_hi:[1,0,0]
	v_fma_mix_f32 v34, v17, v22, s23 op_sel:[1,0,0] op_sel_hi:[1,0,0]
	s_nop 0
	v_lshl_add_u32 v33, v34, 16, v33
	ds_add_u32 v32, v33 offset:192
	v_mov_b32_e32 v26, 0
	s_nop 1
	v_mov_b32_dpp v26, v31 row_newbcast:3 row_mask:0xf bank_mask:0xf
	v_lshlrev_b32_e32 v35, 8, v26
	v_and_or_b32 v35, v35, s22, v24
	s_waitcnt vmcnt(1)
	global_load_dwordx4 v[14:17], v35, s[12:13]
	s_add_i32 s1, s1, 1
	s_add_i32 s0, s0, 16
	s_cmp_lt_u32 s1, s21
	s_cbranch_scc1 .Lagg_loop
